# baseline (speedup 1.0000x reference)
_Z8k_layer1PKDF16_PKiS2_PiS3_PKDv4_jS6_PKfS8_P15HIP_vector_typeIfLj2EESB_:
	s_load_dwordx16 s[8:23], s[0:1], 0x0
	s_load_dwordx4 s[24:27], s[0:1], 0x40
	s_load_dwordx2 s[28:29], s[0:1], 0x50
	s_and_b32 s3, s2, 7
	s_lshl_b32 s3, s3, 7
	s_lshr_b32 s4, s2, 3
	s_add_i32 s3, s3, s4
	s_cmpk_gt_u32 s3, 0x3fc
	s_cbranch_scc1 .Lk2f_exit
	v_lshrrev_b32_e32 v1, 6, v0
	v_lshlrev_b32_e32 v2, 4, v0
	v_readfirstlane_b32 s4, v1
	v_mov_b32_e32 v4, 0xffffff
	v_mov_b32_e32 v5, 0xffffff
	v_mov_b32_e32 v6, 0xffffff
	v_mov_b32_e32 v7, 0xffffff
	ds_write_b128 v2, v[4:7] offset:19456
	s_movk_i32 s5, 0x17b
	v_cmp_gt_u32_e32 vcc, s5, v0
	s_and_saveexec_b64 s[6:7], vcc
	s_cbranch_execz .Lk2f_i1
	ds_write_b128 v2, v[4:7] offset:27648
.Lk2f_i1:
	s_mov_b64 exec, s[6:7]
	s_movk_i32 s5, 0x80
	v_cmp_gt_u32_e32 vcc, s5, v0
	v_lshlrev_b32_e32 v3, 2, v0
	v_mov_b32_e32 v8, 0
	s_and_saveexec_b64 s[6:7], vcc
	s_cbranch_execz .Lk2f_i2
	ds_write_b32 v3, v8 offset:18688
.Lk2f_i2:
	s_mov_b64 exec, s[6:7]
	s_waitcnt lgkmcnt(0)
	v_add_u32_e32 v9, 0x2000, v2
	global_load_dwordx4 v[10:13], v2, s[18:19]
	global_load_dwordx4 v[14:17], v9, s[18:19]
	s_load_dwordx2 s[36:37], s[24:25], 0x0
	s_cmp_lt_u32 s4, 2
	s_cbranch_scc0 .Lk2f_l1
	global_load_dwordx4 v[18:21], v2, s[20:21]
.Lk2f_l1:
	s_cmp_eq_u32 s4, 4
	s_cbranch_scc0 .Lk2f_l2
	v_and_b32_e32 v22, 63, v0
	v_cmp_gt_u32_e32 vcc, 16, v22
	v_lshlrev_b32_e32 v22, 4, v22
	s_and_saveexec_b64 s[6:7], vcc
	global_load_dwordx4 v[18:21], v22, s[22:23]
	s_mov_b64 exec, s[6:7]
.Lk2f_l2:
	v_mov_b32_e32 v8, 0
	v_mov_b32_e32 v9, 0
	s_cmp_lt_u32 s4, 4
	s_cbranch_scc0 .Lk2f_l3
	s_movk_i32 s5, 0xf5
	v_cmp_gt_u32_e32 vcc, s5, v0
	v_mov_b32_e32 v23, s3
	s_movk_i32 s5, 0x3fe
	v_mad_u32_u24 v23, v0, s5, v23
	v_lshlrev_b32_e32 v23, 2, v23
	s_and_saveexec_b64 s[6:7], vcc
	global_load_dwordx2 v[8:9], v23, s[12:13]
	s_mov_b64 exec, s[6:7]
.Lk2f_l3:
	s_waitcnt vmcnt(0)
	s_cmp_lt_u32 s4, 4
	s_cbranch_scc0 .Lk2f_l4
	v_sub_u32_e32 v24, v9, v8
	v_min_u32_e32 v25, 0xf4, v0
	v_lshlrev_b32_e32 v25, 14, v25
	v_lshl_add_u32 v25, v8, 2, v25
	global_load_dwordx4 v[26:29], v25, s[10:11]
	global_load_dwordx4 v[30:33], v25, s[10:11] offset:16
	global_load_dwordx4 v[34:37], v25, s[10:11] offset:32
	global_load_dwordx4 v[38:41], v25, s[10:11] offset:48
	v_add_u32_dpp v42, v8, v8 row_shr:1 row_mask:0xf bank_mask:0xf bound_ctrl:1
	s_nop 1
	v_add_u32_dpp v42, v42, v42 row_shr:2 row_mask:0xf bank_mask:0xf bound_ctrl:1
	s_nop 1
	v_add_u32_dpp v42, v42, v42 row_shr:4 row_mask:0xf bank_mask:0xf bound_ctrl:1
	s_nop 1
	v_add_u32_dpp v42, v42, v42 row_shr:8 row_mask:0xf bank_mask:0xf bound_ctrl:1
	s_nop 1
	v_add_u32_dpp v42, v42, v42 row_bcast:15 row_mask:0xa bank_mask:0xf
	s_nop 1
	v_add_u32_dpp v42, v42, v42 row_bcast:31 row_mask:0xc bank_mask:0xf
	s_lshl_b32 s5, s4, 2
	v_mov_b32_e32 v43, s5
	v_readlane_b32 s5, v42, 63
	s_nop 3
	v_mov_b32_e32 v42, s5
	ds_write_b32 v43, v42 offset:19216
.Lk2f_l4:
	ds_write_b128 v2, v[10:13]
	ds_write_b128 v2, v[14:17] offset:8192
	s_cmp_lt_u32 s4, 2
	s_cbranch_scc0 .Lk2f_l5
	ds_write_b128 v2, v[18:21] offset:16384
.Lk2f_l5:
	s_cmp_eq_u32 s4, 4
	s_cbranch_scc0 .Lk2f_l6
	v_and_b32_e32 v23, 63, v0
	v_cmp_gt_u32_e32 vcc, 16, v23
	s_and_saveexec_b64 s[6:7], vcc
	ds_write_b128 v22, v[18:21] offset:18432
	s_mov_b64 exec, s[6:7]
.Lk2f_l6:
	s_waitcnt lgkmcnt(0)
	s_barrier
	s_cmp_lt_u32 s4, 4
	s_cbranch_scc0 .Lk2f_b2
	s_waitcnt vmcnt(0)
	v_mov_b32_e32 v9, 1
	v_cmp_lt_i32_e32 vcc, 0, v24
	s_mov_b64 exec, vcc
	s_cbranch_execz .Lk2f_atd
	v_ashrrev_i32_e32 v42, 17, v26
	v_lshlrev_b32_e32 v42, 2, v42
	ds_add_rtn_u32 v44, v42, v9 offset:18688
	v_cmp_lt_i32_e32 vcc, 1, v24
	s_mov_b64 exec, vcc
	s_cbranch_execz .Lk2f_atd
	v_ashrrev_i32_e32 v43, 17, v27
	v_lshlrev_b32_e32 v43, 2, v43
	ds_add_rtn_u32 v45, v43, v9 offset:18688
	v_cmp_lt_i32_e32 vcc, 2, v24
	s_mov_b64 exec, vcc
	s_cbranch_execz .Lk2f_atd
	v_ashrrev_i32_e32 v42, 17, v28
	v_lshlrev_b32_e32 v42, 2, v42
	ds_add_rtn_u32 v46, v42, v9 offset:18688
	v_cmp_lt_i32_e32 vcc, 3, v24
	s_mov_b64 exec, vcc
	s_cbranch_execz .Lk2f_atd
	v_ashrrev_i32_e32 v43, 17, v29
	v_lshlrev_b32_e32 v43, 2, v43
	ds_add_rtn_u32 v47, v43, v9 offset:18688
	v_cmp_lt_i32_e32 vcc, 4, v24
	s_mov_b64 exec, vcc
	s_cbranch_execz .Lk2f_atd
	v_ashrrev_i32_e32 v42, 17, v30
	v_lshlrev_b32_e32 v42, 2, v42
	ds_add_rtn_u32 v48, v42, v9 offset:18688
	v_cmp_lt_i32_e32 vcc, 5, v24
	s_mov_b64 exec, vcc
	s_cbranch_execz .Lk2f_atd
	v_ashrrev_i32_e32 v43, 17, v31
	v_lshlrev_b32_e32 v43, 2, v43
	ds_add_rtn_u32 v49, v43, v9 offset:18688
	v_cmp_lt_i32_e32 vcc, 6, v24
	s_mov_b64 exec, vcc
	s_cbranch_execz .Lk2f_atd
	v_ashrrev_i32_e32 v42, 17, v32
	v_lshlrev_b32_e32 v42, 2, v42
	ds_add_rtn_u32 v50, v42, v9 offset:18688
	v_cmp_lt_i32_e32 vcc, 7, v24
	s_mov_b64 exec, vcc
	s_cbranch_execz .Lk2f_atd
	v_ashrrev_i32_e32 v43, 17, v33
	v_lshlrev_b32_e32 v43, 2, v43
	ds_add_rtn_u32 v51, v43, v9 offset:18688
	v_cmp_lt_i32_e32 vcc, 8, v24
	s_mov_b64 exec, vcc
	s_cbranch_execz .Lk2f_atd
	v_ashrrev_i32_e32 v42, 17, v34
	v_lshlrev_b32_e32 v42, 2, v42
	ds_add_rtn_u32 v52, v42, v9 offset:18688
	v_cmp_lt_i32_e32 vcc, 9, v24
	s_mov_b64 exec, vcc
	s_cbranch_execz .Lk2f_atd
	v_ashrrev_i32_e32 v43, 17, v35
	v_lshlrev_b32_e32 v43, 2, v43
	ds_add_rtn_u32 v53, v43, v9 offset:18688
	v_cmp_lt_i32_e32 vcc, 10, v24
	s_mov_b64 exec, vcc
	s_cbranch_execz .Lk2f_atd
	v_ashrrev_i32_e32 v42, 17, v36
	v_lshlrev_b32_e32 v42, 2, v42
	ds_add_rtn_u32 v54, v42, v9 offset:18688
	v_cmp_lt_i32_e32 vcc, 11, v24
	s_mov_b64 exec, vcc
	s_cbranch_execz .Lk2f_atd
	v_ashrrev_i32_e32 v43, 17, v37
	v_lshlrev_b32_e32 v43, 2, v43
	ds_add_rtn_u32 v55, v43, v9 offset:18688
	v_cmp_lt_i32_e32 vcc, 12, v24
	s_mov_b64 exec, vcc
	s_cbranch_execz .Lk2f_atd
	v_ashrrev_i32_e32 v42, 17, v38
	v_lshlrev_b32_e32 v42, 2, v42
	ds_add_rtn_u32 v56, v42, v9 offset:18688
	v_cmp_lt_i32_e32 vcc, 13, v24
	s_mov_b64 exec, vcc
	s_cbranch_execz .Lk2f_atd
	v_ashrrev_i32_e32 v43, 17, v39
	v_lshlrev_b32_e32 v43, 2, v43
	ds_add_rtn_u32 v57, v43, v9 offset:18688
	v_cmp_lt_i32_e32 vcc, 14, v24
	s_mov_b64 exec, vcc
	s_cbranch_execz .Lk2f_atd
	v_ashrrev_i32_e32 v42, 17, v40
	v_lshlrev_b32_e32 v42, 2, v42
	ds_add_rtn_u32 v58, v42, v9 offset:18688
	v_cmp_lt_i32_e32 vcc, 15, v24
	s_mov_b64 exec, vcc
	s_cbranch_execz .Lk2f_atd
	v_ashrrev_i32_e32 v43, 17, v41
	v_lshlrev_b32_e32 v43, 2, v43
	ds_add_rtn_u32 v59, v43, v9 offset:18688
.Lk2f_atd:
	s_mov_b64 exec, -1
	s_waitcnt lgkmcnt(0)
	v_cmp_lt_i32_e32 vcc, 0, v24
	s_mov_b64 exec, vcc
	s_cbranch_execz .Lk2f_sld
	v_ashrrev_i32_e32 v42, 17, v26
	v_min_u32_e32 v44, 35, v44
	v_mul_u32_u24_e32 v42, 0x90, v42
	v_and_b32_e32 v43, 0x1ffff, v26
	v_lshl_add_u32 v42, v44, 2, v42
	ds_write_b32 v42, v43 offset:19456
	v_cmp_lt_i32_e32 vcc, 1, v24
	s_mov_b64 exec, vcc
	s_cbranch_execz .Lk2f_sld
	v_ashrrev_i32_e32 v42, 17, v27
	v_min_u32_e32 v45, 35, v45
	v_mul_u32_u24_e32 v42, 0x90, v42
	v_and_b32_e32 v43, 0x1ffff, v27
	v_lshl_add_u32 v42, v45, 2, v42
	ds_write_b32 v42, v43 offset:19456
	v_cmp_lt_i32_e32 vcc, 2, v24
	s_mov_b64 exec, vcc
	s_cbranch_execz .Lk2f_sld
	v_ashrrev_i32_e32 v42, 17, v28
	v_min_u32_e32 v46, 35, v46
	v_mul_u32_u24_e32 v42, 0x90, v42
	v_and_b32_e32 v43, 0x1ffff, v28
	v_lshl_add_u32 v42, v46, 2, v42
	ds_write_b32 v42, v43 offset:19456
	v_cmp_lt_i32_e32 vcc, 3, v24
	s_mov_b64 exec, vcc
	s_cbranch_execz .Lk2f_sld
	v_ashrrev_i32_e32 v42, 17, v29
	v_min_u32_e32 v47, 35, v47
	v_mul_u32_u24_e32 v42, 0x90, v42
	v_and_b32_e32 v43, 0x1ffff, v29
	v_lshl_add_u32 v42, v47, 2, v42
	ds_write_b32 v42, v43 offset:19456
	v_cmp_lt_i32_e32 vcc, 4, v24
	s_mov_b64 exec, vcc
	s_cbranch_execz .Lk2f_sld
	v_ashrrev_i32_e32 v42, 17, v30
	v_min_u32_e32 v48, 35, v48
	v_mul_u32_u24_e32 v42, 0x90, v42
	v_and_b32_e32 v43, 0x1ffff, v30
	v_lshl_add_u32 v42, v48, 2, v42
	ds_write_b32 v42, v43 offset:19456
	v_cmp_lt_i32_e32 vcc, 5, v24
	s_mov_b64 exec, vcc
	s_cbranch_execz .Lk2f_sld
	v_ashrrev_i32_e32 v42, 17, v31
	v_min_u32_e32 v49, 35, v49
	v_mul_u32_u24_e32 v42, 0x90, v42
	v_and_b32_e32 v43, 0x1ffff, v31
	v_lshl_add_u32 v42, v49, 2, v42
	ds_write_b32 v42, v43 offset:19456
	v_cmp_lt_i32_e32 vcc, 6, v24
	s_mov_b64 exec, vcc
	s_cbranch_execz .Lk2f_sld
	v_ashrrev_i32_e32 v42, 17, v32
	v_min_u32_e32 v50, 35, v50
	v_mul_u32_u24_e32 v42, 0x90, v42
	v_and_b32_e32 v43, 0x1ffff, v32
	v_lshl_add_u32 v42, v50, 2, v42
	ds_write_b32 v42, v43 offset:19456
	v_cmp_lt_i32_e32 vcc, 7, v24
	s_mov_b64 exec, vcc
	s_cbranch_execz .Lk2f_sld
	v_ashrrev_i32_e32 v42, 17, v33
	v_min_u32_e32 v51, 35, v51
	v_mul_u32_u24_e32 v42, 0x90, v42
	v_and_b32_e32 v43, 0x1ffff, v33
	v_lshl_add_u32 v42, v51, 2, v42
	ds_write_b32 v42, v43 offset:19456
	v_cmp_lt_i32_e32 vcc, 8, v24
	s_mov_b64 exec, vcc
	s_cbranch_execz .Lk2f_sld
	v_ashrrev_i32_e32 v42, 17, v34
	v_min_u32_e32 v52, 35, v52
	v_mul_u32_u24_e32 v42, 0x90, v42
	v_and_b32_e32 v43, 0x1ffff, v34
	v_lshl_add_u32 v42, v52, 2, v42
	ds_write_b32 v42, v43 offset:19456
	v_cmp_lt_i32_e32 vcc, 9, v24
	s_mov_b64 exec, vcc
	s_cbranch_execz .Lk2f_sld
	v_ashrrev_i32_e32 v42, 17, v35
	v_min_u32_e32 v53, 35, v53
	v_mul_u32_u24_e32 v42, 0x90, v42
	v_and_b32_e32 v43, 0x1ffff, v35
	v_lshl_add_u32 v42, v53, 2, v42
	ds_write_b32 v42, v43 offset:19456
	v_cmp_lt_i32_e32 vcc, 10, v24
	s_mov_b64 exec, vcc
	s_cbranch_execz .Lk2f_sld
	v_ashrrev_i32_e32 v42, 17, v36
	v_min_u32_e32 v54, 35, v54
	v_mul_u32_u24_e32 v42, 0x90, v42
	v_and_b32_e32 v43, 0x1ffff, v36
	v_lshl_add_u32 v42, v54, 2, v42
	ds_write_b32 v42, v43 offset:19456
	v_cmp_lt_i32_e32 vcc, 11, v24
	s_mov_b64 exec, vcc
	s_cbranch_execz .Lk2f_sld
	v_ashrrev_i32_e32 v42, 17, v37
	v_min_u32_e32 v55, 35, v55
	v_mul_u32_u24_e32 v42, 0x90, v42
	v_and_b32_e32 v43, 0x1ffff, v37
	v_lshl_add_u32 v42, v55, 2, v42
	ds_write_b32 v42, v43 offset:19456
	v_cmp_lt_i32_e32 vcc, 12, v24
	s_mov_b64 exec, vcc
	s_cbranch_execz .Lk2f_sld
	v_ashrrev_i32_e32 v42, 17, v38
	v_min_u32_e32 v56, 35, v56
	v_mul_u32_u24_e32 v42, 0x90, v42
	v_and_b32_e32 v43, 0x1ffff, v38
	v_lshl_add_u32 v42, v56, 2, v42
	ds_write_b32 v42, v43 offset:19456
	v_cmp_lt_i32_e32 vcc, 13, v24
	s_mov_b64 exec, vcc
	s_cbranch_execz .Lk2f_sld
	v_ashrrev_i32_e32 v42, 17, v39
	v_min_u32_e32 v57, 35, v57
	v_mul_u32_u24_e32 v42, 0x90, v42
	v_and_b32_e32 v43, 0x1ffff, v39
	v_lshl_add_u32 v42, v57, 2, v42
	ds_write_b32 v42, v43 offset:19456
	v_cmp_lt_i32_e32 vcc, 14, v24
	s_mov_b64 exec, vcc
	s_cbranch_execz .Lk2f_sld
	v_ashrrev_i32_e32 v42, 17, v40
	v_min_u32_e32 v58, 35, v58
	v_mul_u32_u24_e32 v42, 0x90, v42
	v_and_b32_e32 v43, 0x1ffff, v40
	v_lshl_add_u32 v42, v58, 2, v42
	ds_write_b32 v42, v43 offset:19456
	v_cmp_lt_i32_e32 vcc, 15, v24
	s_mov_b64 exec, vcc
	s_cbranch_execz .Lk2f_sld
	v_ashrrev_i32_e32 v42, 17, v41
	v_min_u32_e32 v59, 35, v59
	v_mul_u32_u24_e32 v42, 0x90, v42
	v_and_b32_e32 v43, 0x1ffff, v41
	v_lshl_add_u32 v42, v59, 2, v42
	ds_write_b32 v42, v43 offset:19456
.Lk2f_sld:
	s_mov_b64 exec, -1
	v_cmp_lt_i32_e32 vcc, 16, v24
	s_and_saveexec_b64 s[6:7], vcc
	s_cbranch_execz .Lk2f_lgd
	v_add_u32_e32 v25, 64, v25
	v_add_u32_e32 v24, -16, v24
.Lk2f_lg:
	global_load_dword v43, v25, s[10:11]
	v_add_u32_e32 v25, 4, v25
	v_add_u32_e32 v24, -1, v24
	s_waitcnt vmcnt(0)
	v_ashrrev_i32_e32 v42, 17, v43
	v_lshlrev_b32_e32 v44, 2, v42
	ds_add_rtn_u32 v44, v44, v9 offset:18688
	v_mul_u32_u24_e32 v42, 0x90, v42
	v_and_b32_e32 v43, 0x1ffff, v43
	v_cmp_lt_i32_e32 vcc, 0, v24
	s_waitcnt lgkmcnt(0)
	v_min_u32_e32 v44, 35, v44
	v_lshl_add_u32 v42, v44, 2, v42
	ds_write_b32 v42, v43 offset:19456
	s_and_b64 exec, exec, vcc
	s_cbranch_execnz .Lk2f_lg
.Lk2f_lgd:
	s_mov_b64 exec, -1
.Lk2f_b2:
	s_waitcnt lgkmcnt(0)
	s_barrier
	v_and_b32_e32 v1, 63, v0
	v_lshlrev_b32_e32 v6, 3, v1
	ds_read_b64 v[14:15], v6 offset:18688
	s_cmp_eq_u32 s4, 7
	s_cbranch_scc1 .Lk2f_w7
	v_lshrrev_b32_e32 v3, 2, v1
	s_mul_i32 s5, s4, 14
	v_add_u32_e32 v6, s5, v3
	v_cmp_gt_u32_e32 vcc, 14, v3
	v_mov_b32_e32 v7, 0x7f
	v_mov_b32_e32 v8, 0x62
	v_and_b32_e32 v9, 3, v1
	v_cndmask_b32_e32 v7, v7, v6, vcc
	v_cndmask_b32_e32 v8, v8, v6, vcc
	v_lshlrev_b32_e32 v7, 2, v7
	v_mul_u32_u24_e32 v2, 0x90, v8
	ds_read_b32 v3, v7 offset:18688
	ds_read_b128 v[4:7], v2 offset:19456
	v_lshlrev_b32_e32 v1, 4, v9
	s_mov_b32 s32, s8
	s_and_b32 s33, s9, 0xffff
	s_mov_b32 s34, 0xc35000
	s_mov_b32 s35, 0x20000
	v_and_b32_e32 v8, 15, v0
	v_add_u32_e32 v9, s5, v8
	s_mul_i32 s6, s3, 0x62
	v_add_u32_e32 v9, s6, v9
	v_cmp_gt_u32_e32 vcc, 14, v8
	s_mov_b32 s7, 0x186a0
	v_cmp_gt_u32_e64 s[38:39], s7, v9
	s_and_b64 vcc, vcc, s[38:39]
	s_mov_b64 s[40:41], vcc
	v_and_b32_e32 v8, 0x30, v0
	v_cndmask_b32_e32 v9, 0, v9, vcc
	v_lshl_or_b32 v8, v9, 7, v8
	buffer_load_dwordx4 v[56:59], v8, s[32:35], 0 offen
	buffer_load_dwordx4 v[60:63], v8, s[32:35], 0 offen offset:64
	v_mov_b32_e32 v40, 0
	v_mov_b32_e32 v41, 0
	v_mov_b32_e32 v42, 0
	v_mov_b32_e32 v43, 0
	v_mov_b32_e32 v44, 0
	v_mov_b32_e32 v45, 0
	v_mov_b32_e32 v46, 0
	v_mov_b32_e32 v47, 0
	v_mov_b32_e32 v48, 0
	v_mov_b32_e32 v49, 0
	v_mov_b32_e32 v50, 0
	v_mov_b32_e32 v51, 0
	v_mov_b32_e32 v52, 0
	v_mov_b32_e32 v53, 0
	v_mov_b32_e32 v54, 0
	v_mov_b32_e32 v55, 0
	s_mov_b32 s5, 0
	s_waitcnt lgkmcnt(0)
	v_max_u32_e32 v8, v14, v15
	v_cmp_lt_u32_e32 vcc, 32, v8
	s_cmp_lg_u64 vcc, 0
	s_cbranch_scc1 .Lk2f_fallback
	v_cmp_lt_i32_e32 vcc, 0, v3
	s_cmp_lg_u64 vcc, 0
	s_cbranch_scc0 .Lk2f_gdone
.Lk2f_loop:
	v_lshl_or_b32 v4, v4, 7, v1
	v_lshl_or_b32 v5, v5, 7, v1
	v_lshl_or_b32 v6, v6, 7, v1
	v_lshl_or_b32 v7, v7, 7, v1
	buffer_load_dwordx4 v[8:11], v4, s[32:35], 0 offen
	buffer_load_dwordx4 v[12:15], v4, s[32:35], 0 offen offset:64
	buffer_load_dwordx4 v[16:19], v5, s[32:35], 0 offen
	buffer_load_dwordx4 v[20:23], v5, s[32:35], 0 offen offset:64
	buffer_load_dwordx4 v[24:27], v6, s[32:35], 0 offen
	buffer_load_dwordx4 v[28:31], v6, s[32:35], 0 offen offset:64
	buffer_load_dwordx4 v[32:35], v7, s[32:35], 0 offen
	buffer_load_dwordx4 v[36:39], v7, s[32:35], 0 offen offset:64
	v_add_u32_e32 v2, 16, v2
	s_add_i32 s5, s5, 4
	ds_read_b128 v[4:7], v2 offset:19456
	v_cmp_lt_i32_e32 vcc, s5, v3
	s_waitcnt vmcnt(5)
	v_pk_add_f16 v8, v8, v16
	v_pk_add_f16 v9, v9, v17
	v_pk_add_f16 v10, v10, v18
	v_pk_add_f16 v11, v11, v19
	s_waitcnt vmcnt(4)
	v_pk_add_f16 v12, v12, v20
	v_pk_add_f16 v13, v13, v21
	v_pk_add_f16 v14, v14, v22
	v_pk_add_f16 v15, v15, v23
	s_waitcnt vmcnt(1)
	v_pk_add_f16 v24, v24, v32
	v_pk_add_f16 v25, v25, v33
	v_pk_add_f16 v26, v26, v34
	v_pk_add_f16 v27, v27, v35
	v_pk_add_f16 v8, v8, v24
	v_pk_add_f16 v9, v9, v25
	v_pk_add_f16 v10, v10, v26
	v_pk_add_f16 v11, v11, v27
	s_waitcnt vmcnt(0)
	v_pk_add_f16 v28, v28, v36
	v_pk_add_f16 v29, v29, v37
	v_pk_add_f16 v30, v30, v38
	v_pk_add_f16 v31, v31, v39
	v_pk_add_f16 v12, v12, v28
	v_pk_add_f16 v13, v13, v29
	v_pk_add_f16 v14, v14, v30
	v_pk_add_f16 v15, v15, v31
	v_fma_mix_f32 v40, v8, 1.0, v40 op_sel:[0,0,0] op_sel_hi:[1,0,0]
	v_fma_mix_f32 v41, v8, 1.0, v41 op_sel:[1,0,0] op_sel_hi:[1,0,0]
	v_fma_mix_f32 v42, v9, 1.0, v42 op_sel:[0,0,0] op_sel_hi:[1,0,0]
	v_fma_mix_f32 v43, v9, 1.0, v43 op_sel:[1,0,0] op_sel_hi:[1,0,0]
	v_fma_mix_f32 v44, v10, 1.0, v44 op_sel:[0,0,0] op_sel_hi:[1,0,0]
	v_fma_mix_f32 v45, v10, 1.0, v45 op_sel:[1,0,0] op_sel_hi:[1,0,0]
	v_fma_mix_f32 v46, v11, 1.0, v46 op_sel:[0,0,0] op_sel_hi:[1,0,0]
	v_fma_mix_f32 v47, v11, 1.0, v47 op_sel:[1,0,0] op_sel_hi:[1,0,0]
	v_fma_mix_f32 v48, v12, 1.0, v48 op_sel:[0,0,0] op_sel_hi:[1,0,0]
	v_fma_mix_f32 v49, v12, 1.0, v49 op_sel:[1,0,0] op_sel_hi:[1,0,0]
	v_fma_mix_f32 v50, v13, 1.0, v50 op_sel:[0,0,0] op_sel_hi:[1,0,0]
	v_fma_mix_f32 v51, v13, 1.0, v51 op_sel:[1,0,0] op_sel_hi:[1,0,0]
	v_fma_mix_f32 v52, v14, 1.0, v52 op_sel:[0,0,0] op_sel_hi:[1,0,0]
	v_fma_mix_f32 v53, v14, 1.0, v53 op_sel:[1,0,0] op_sel_hi:[1,0,0]
	v_fma_mix_f32 v54, v15, 1.0, v54 op_sel:[0,0,0] op_sel_hi:[1,0,0]
	v_fma_mix_f32 v55, v15, 1.0, v55 op_sel:[1,0,0] op_sel_hi:[1,0,0]
	s_waitcnt lgkmcnt(0)
	s_cmp_lg_u64 vcc, 0
	s_cbranch_scc1 .Lk2f_loop
.Lk2f_gdone:
	v_and_b32_e32 v2, 63, v0
	v_lshrrev_b32_e32 v5, 4, v2
	v_lshlrev_b32_e32 v7, 4, v5
	v_lshlrev_b32_e32 v6, 4, v2
	ds_read_b128 v[24:27], v7 offset:18432
	ds_read_b128 v[28:31], v7 offset:18496
	ds_read_b128 v[32:35], v7 offset:18560
	ds_read_b128 v[36:39], v7 offset:18624
	v_and_b32_e32 v16, 15, v2
	v_lshl_or_b32 v5, v16, 2, v5
	v_lshlrev_b32_e32 v5, 2, v5
	v_cvt_f32_i32_e32 v4, v3
	v_max_f32_e32 v4, 1.0, v4
	v_div_scale_f32 v16, s[6:7], v4, v4, 1.0
	v_rcp_f32_e32 v17, v16
	s_nop 0
	v_fma_f32 v18, -v16, v17, 1.0
	v_fmac_f32_e32 v17, v18, v17
	v_div_scale_f32 v18, vcc, 1.0, v4, 1.0
	v_mul_f32_e32 v19, v18, v17
	v_fma_f32 v8, -v16, v19, v18
	v_fmac_f32_e32 v19, v8, v17
	v_fma_f32 v16, -v16, v19, v18
	v_div_fmas_f32 v16, v16, v17, v19
	v_div_fixup_f32 v4, v16, v4, 1.0
	v_mul_f32_e32 v40, v4, v40
	v_mul_f32_e32 v41, v4, v41
	v_mul_f32_e32 v42, v4, v42
	v_mul_f32_e32 v43, v4, v43
	v_mul_f32_e32 v44, v4, v44
	v_mul_f32_e32 v45, v4, v45
	v_mul_f32_e32 v46, v4, v46
	v_mul_f32_e32 v47, v4, v47
	v_mul_f32_e32 v48, v4, v48
	v_mul_f32_e32 v49, v4, v49
	v_mul_f32_e32 v50, v4, v50
	v_mul_f32_e32 v51, v4, v51
	v_mul_f32_e32 v52, v4, v52
	v_mul_f32_e32 v53, v4, v53
	v_mul_f32_e32 v54, v4, v54
	v_mul_f32_e32 v55, v4, v55
	v_cvt_pk_f16_f32 v8, v40, v41
	v_cvt_pk_f16_f32 v9, v42, v43
	v_cvt_pk_f16_f32 v10, v44, v45
	v_cvt_pk_f16_f32 v11, v46, v47
	v_cvt_pk_f16_f32 v12, v48, v49
	v_cvt_pk_f16_f32 v13, v50, v51
	v_cvt_pk_f16_f32 v14, v52, v53
	v_cvt_pk_f16_f32 v15, v54, v55
	s_waitcnt lgkmcnt(0)
	ds_bpermute_b32 v16, v5, v8
	ds_bpermute_b32 v17, v5, v9
	ds_bpermute_b32 v18, v5, v10
	ds_bpermute_b32 v19, v5, v11
	ds_bpermute_b32 v20, v5, v12
	ds_bpermute_b32 v21, v5, v13
	ds_bpermute_b32 v22, v5, v14
	ds_bpermute_b32 v23, v5, v15
	ds_read_b128 v[40:43], v6 offset:0
	ds_read_b128 v[44:47], v6 offset:1024
	ds_read_b128 v[48:51], v6 offset:2048
	ds_read_b128 v[52:55], v6 offset:3072
	s_waitcnt vmcnt(0)
	s_waitcnt lgkmcnt(3)
	v_mfma_f32_16x16x32_f16 v[24:27], v[40:43], v[16:19], v[24:27]
	s_waitcnt lgkmcnt(2)
	v_mfma_f32_16x16x32_f16 v[24:27], v[44:47], v[20:23], v[24:27]
	s_waitcnt lgkmcnt(1)
	v_mfma_f32_16x16x32_f16 v[24:27], v[48:51], v[56:59], v[24:27]
	s_waitcnt lgkmcnt(0)
	v_mfma_f32_16x16x32_f16 v[24:27], v[52:55], v[60:63], v[24:27]
	ds_read_b128 v[40:43], v6 offset:4096
	ds_read_b128 v[44:47], v6 offset:5120
	ds_read_b128 v[48:51], v6 offset:6144
	ds_read_b128 v[52:55], v6 offset:7168
	s_waitcnt lgkmcnt(3)
	v_mfma_f32_16x16x32_f16 v[28:31], v[40:43], v[16:19], v[28:31]
	s_waitcnt lgkmcnt(2)
	v_mfma_f32_16x16x32_f16 v[28:31], v[44:47], v[20:23], v[28:31]
	s_waitcnt lgkmcnt(1)
	v_mfma_f32_16x16x32_f16 v[28:31], v[48:51], v[56:59], v[28:31]
	s_waitcnt lgkmcnt(0)
	v_mfma_f32_16x16x32_f16 v[28:31], v[52:55], v[60:63], v[28:31]
	ds_read_b128 v[40:43], v6 offset:8192
	ds_read_b128 v[44:47], v6 offset:9216
	ds_read_b128 v[48:51], v6 offset:10240
	ds_read_b128 v[52:55], v6 offset:11264
	s_waitcnt lgkmcnt(3)
	v_mfma_f32_16x16x32_f16 v[32:35], v[40:43], v[16:19], v[32:35]
	s_waitcnt lgkmcnt(2)
	v_mfma_f32_16x16x32_f16 v[32:35], v[44:47], v[20:23], v[32:35]
	s_waitcnt lgkmcnt(1)
	v_mfma_f32_16x16x32_f16 v[32:35], v[48:51], v[56:59], v[32:35]
	s_waitcnt lgkmcnt(0)
	v_mfma_f32_16x16x32_f16 v[32:35], v[52:55], v[60:63], v[32:35]
	ds_read_b128 v[40:43], v6 offset:12288
	ds_read_b128 v[44:47], v6 offset:13312
	ds_read_b128 v[48:51], v6 offset:14336
	ds_read_b128 v[52:55], v6 offset:15360
	s_waitcnt lgkmcnt(3)
	v_mfma_f32_16x16x32_f16 v[36:39], v[40:43], v[16:19], v[36:39]
	s_waitcnt lgkmcnt(2)
	v_mfma_f32_16x16x32_f16 v[36:39], v[44:47], v[20:23], v[36:39]
	s_waitcnt lgkmcnt(1)
	v_mfma_f32_16x16x32_f16 v[36:39], v[48:51], v[56:59], v[36:39]
	s_waitcnt lgkmcnt(0)
	v_mfma_f32_16x16x32_f16 v[36:39], v[52:55], v[60:63], v[36:39]
	ds_read_b128 v[40:43], v6 offset:16384
	ds_read_b128 v[44:47], v6 offset:17408
	v_max_f32_e32 v24, 0, v24
	v_max_f32_e32 v25, 0, v25
	v_max_f32_e32 v26, 0, v26
	v_max_f32_e32 v27, 0, v27
	v_cvt_pk_f16_f32 v8, v24, v25
	v_cvt_pk_f16_f32 v9, v26, v27
	v_max_f32_e32 v28, 0, v28
	v_max_f32_e32 v29, 0, v29
	v_max_f32_e32 v30, 0, v30
	v_max_f32_e32 v31, 0, v31
	v_cvt_pk_f16_f32 v10, v28, v29
	v_cvt_pk_f16_f32 v11, v30, v31
	v_max_f32_e32 v32, 0, v32
	v_max_f32_e32 v33, 0, v33
	v_max_f32_e32 v34, 0, v34
	v_max_f32_e32 v35, 0, v35
	v_cvt_pk_f16_f32 v12, v32, v33
	v_cvt_pk_f16_f32 v13, v34, v35
	v_max_f32_e32 v36, 0, v36
	v_max_f32_e32 v37, 0, v37
	v_max_f32_e32 v38, 0, v38
	v_max_f32_e32 v39, 0, v39
	v_cvt_pk_f16_f32 v14, v36, v37
	v_cvt_pk_f16_f32 v15, v38, v39
	v_mov_b32_e32 v4, 0
	v_mov_b32_e32 v5, 0
	v_mov_b32_e32 v6, s36
	v_mov_b32_e32 v7, s37
	s_waitcnt lgkmcnt(0)
	s_nop 1
	v_mfma_f32_16x16x32_f16 v[4:7], v[40:43], v[8:11], v[4:7]
	v_mfma_f32_16x16x32_f16 v[4:7], v[44:47], v[12:15], v[4:7]
	s_mul_i32 s5, s4, 14
	s_mul_i32 s6, s3, 0x62
	s_add_i32 s5, s5, s6
	v_and_b32_e32 v8, 15, v2
	v_add_u32_e32 v8, s5, v8
	v_lshlrev_b32_e32 v8, 3, v8
	v_cmp_gt_u32_e32 vcc, 16, v2
	s_and_b64 vcc, vcc, s[40:41]
	s_and_saveexec_b64 s[6:7], vcc
	s_cbranch_execz .Lk2f_exit
	s_nop 7
	global_store_dwordx2 v8, v[4:5], s[26:27]
	global_store_dwordx2 v8, v[6:7], s[28:29]
	s_endpgm
.Lk2f_w7:
	v_mov_b32_e32 v8, 0
	ds_read_b128 v[4:7], v8 offset:19216
	s_waitcnt lgkmcnt(0)
	v_max_u32_e32 v9, v14, v15
	v_cmp_lt_u32_e32 vcc, 32, v9
	s_cmp_lg_u64 vcc, 0
	s_cbranch_scc1 .Lk2f_fallback
	v_add3_u32 v4, v4, v5, v6
	v_add_u32_e32 v4, v4, v7
	v_add_u32_e32 v11, v14, v15
	s_nop 1
	v_add_u32_dpp v12, v11, v11 row_shr:1 row_mask:0xf bank_mask:0xf bound_ctrl:1
	s_nop 1
	v_add_u32_dpp v12, v12, v12 row_shr:2 row_mask:0xf bank_mask:0xf bound_ctrl:1
	s_nop 1
	v_add_u32_dpp v12, v12, v12 row_shr:4 row_mask:0xf bank_mask:0xf bound_ctrl:1
	s_nop 1
	v_add_u32_dpp v12, v12, v12 row_shr:8 row_mask:0xf bank_mask:0xf bound_ctrl:1
	s_nop 1
	v_add_u32_dpp v12, v12, v12 row_bcast:15 row_mask:0xa bank_mask:0xf
	s_nop 1
	v_add_u32_dpp v12, v12, v12 row_bcast:31 row_mask:0xc bank_mask:0xf
	v_sub_u32_e32 v12, v12, v11
	v_add_u32_e32 v12, v12, v4
	v_add_u32_e32 v13, v12, v14
	s_mul_i32 s6, s3, 0x62
	v_lshl_add_u32 v16, v1, 1, s6
	s_movk_i32 s7, 49
	v_cmp_gt_u32_e32 vcc, s7, v1
	s_mov_b32 s7, 0x186a0
	v_cmp_gt_u32_e64 s[38:39], s7, v16
	s_and_b64 vcc, vcc, s[38:39]
	v_lshlrev_b32_e32 v17, 2, v16
	s_and_saveexec_b64 s[40:41], vcc
	s_cbranch_execz .Lk2f_w7a
	global_store_dwordx2 v17, v[12:13], s[14:15]
.Lk2f_w7a:
	s_mov_b64 exec, s[40:41]
	s_cmpk_lg_u32 s3, 0x3fc
	s_cbranch_scc1 .Lk2f_w7b
	v_mov_b32_e32 v18, 0x61a80
	v_mov_b32_e32 v19, 0xf4240
	v_cmp_eq_u32_e32 vcc, 0, v1
	s_and_saveexec_b64 s[40:41], vcc
	global_store_dword v18, v19, s[14:15]
	s_mov_b64 exec, s[40:41]
.Lk2f_w7b:
	v_min_u32_e32 v18, 48, v1
	v_mul_u32_u24_e32 v18, 0x120, v18
	v_lshlrev_b32_e32 v12, 2, v12
	v_lshlrev_b32_e32 v13, 2, v13
	v_max_i32_e32 v19, v14, v15
	s_mov_b32 s5, 0
.Lk2f_w7l:
	v_cmp_lt_i32_e32 vcc, s5, v19
	s_cmp_lg_u64 vcc, 0
	s_cbranch_scc0 .Lk2f_exit
	ds_read_b128 v[20:23], v18 offset:19456
	ds_read_b128 v[24:27], v18 offset:19600
	v_subrev_u32_e32 v28, s5, v14
	v_subrev_u32_e32 v29, s5, v15
	s_waitcnt lgkmcnt(0)
	v_cmp_lt_i32_e32 vcc, 0, v28
	s_and_saveexec_b64 s[40:41], vcc
	s_cbranch_execz .Lk2f_w7s0
	global_store_dword v12, v20, s[16:17] offset:0
.Lk2f_w7s0:
	s_mov_b64 exec, s[40:41]
	v_cmp_lt_i32_e32 vcc, 1, v28
	s_and_saveexec_b64 s[40:41], vcc
	s_cbranch_execz .Lk2f_w7s1
	global_store_dword v12, v21, s[16:17] offset:4
.Lk2f_w7s1:
	s_mov_b64 exec, s[40:41]
	v_cmp_lt_i32_e32 vcc, 2, v28
	s_and_saveexec_b64 s[40:41], vcc
	s_cbranch_execz .Lk2f_w7s2
	global_store_dword v12, v22, s[16:17] offset:8
.Lk2f_w7s2:
	s_mov_b64 exec, s[40:41]
	v_cmp_lt_i32_e32 vcc, 3, v28
	s_and_saveexec_b64 s[40:41], vcc
	s_cbranch_execz .Lk2f_w7s3
	global_store_dword v12, v23, s[16:17] offset:12
.Lk2f_w7s3:
	s_mov_b64 exec, s[40:41]
	v_cmp_lt_i32_e32 vcc, 0, v29
	s_and_saveexec_b64 s[40:41], vcc
	s_cbranch_execz .Lk2f_w7t0
	global_store_dword v13, v24, s[16:17] offset:0
.Lk2f_w7t0:
	s_mov_b64 exec, s[40:41]
	v_cmp_lt_i32_e32 vcc, 1, v29
	s_and_saveexec_b64 s[40:41], vcc
	s_cbranch_execz .Lk2f_w7t1
	global_store_dword v13, v25, s[16:17] offset:4
.Lk2f_w7t1:
	s_mov_b64 exec, s[40:41]
	v_cmp_lt_i32_e32 vcc, 2, v29
	s_and_saveexec_b64 s[40:41], vcc
	s_cbranch_execz .Lk2f_w7t2
	global_store_dword v13, v26, s[16:17] offset:8
.Lk2f_w7t2:
	s_mov_b64 exec, s[40:41]
	v_cmp_lt_i32_e32 vcc, 3, v29
	s_and_saveexec_b64 s[40:41], vcc
	s_cbranch_execz .Lk2f_w7t3
	global_store_dword v13, v27, s[16:17] offset:12
.Lk2f_w7t3:
	s_mov_b64 exec, s[40:41]
	v_add_u32_e32 v12, 16, v12
	v_add_u32_e32 v13, 16, v13
	v_add_u32_e32 v18, 16, v18
	s_add_i32 s5, s5, 4
	s_branch .Lk2f_w7l

.Lk2f_fallback:
	s_mov_b64 exec, -1
	s_waitcnt vmcnt(0) lgkmcnt(0)
	s_barrier
.Lk2_orig:
	s_lshl_b32 s3, s2, 7
	s_and_b32 s69, s3, 0x380
	s_lshr_b32 s2, s2, 3
	s_add_i32 s69, s69, s2
	s_cmpk_gt_u32 s69, 0x3fc
	v_readfirstlane_b32 s33, v0
	s_cbranch_scc1 .LBB1_160
	s_load_dwordx2 s[2:3], s[0:1], 0x28
	v_mov_b32_e32 v1, 0
	v_lshlrev_b32_e32 v32, 4, v0
	v_mov_b32_e32 v33, v1
	v_mov_b32_e32 v26, v1
	s_waitcnt lgkmcnt(0)
	v_lshl_add_u64 v[2:3], s[2:3], 0, v[32:33]
	v_add_co_u32_e32 v2, vcc, 0x2000, v2
	v_mov_b32_e32 v27, v1
	s_nop 0
	v_addc_co_u32_e32 v3, vcc, 0, v3, vcc
	global_load_dwordx4 v[18:21], v32, s[2:3]
	global_load_dwordx4 v[22:25], v[2:3], off
	s_movk_i32 s2, 0x7f
	v_cmp_lt_u32_e32 vcc, s2, v0
	s_movk_i32 s2, 0x80
	v_cmp_gt_u32_e64 s[38:39], s2, v0
	v_mov_b32_e32 v28, v1
	v_mov_b32_e32 v29, v1
	s_and_saveexec_b64 s[2:3], s[38:39]
	s_cbranch_execz .LBB1_3
	s_load_dwordx2 s[4:5], s[0:1], 0x30
	s_waitcnt lgkmcnt(0)
	global_load_dwordx4 v[26:29], v32, s[4:5]

	.amdhsa_kernel _Z8k_layer1PKDF16_PKiS2_PiS3_PKDv4_jS6_PKfS8_P15HIP_vector_typeIfLj2EESB_
		.amdhsa_group_segment_fixed_size 33712
		.amdhsa_private_segment_fixed_size 0
		.amdhsa_kernarg_size 88
		.amdhsa_user_sgpr_count 2
		.amdhsa_user_sgpr_dispatch_ptr 0
		.amdhsa_user_sgpr_queue_ptr 0
		.amdhsa_user_sgpr_kernarg_segment_ptr 1
		.amdhsa_user_sgpr_dispatch_id 0
		.amdhsa_user_sgpr_kernarg_preload_length 0
		.amdhsa_user_sgpr_kernarg_preload_offset 0
		.amdhsa_user_sgpr_private_segment_size 0
		.amdhsa_uses_dynamic_stack 0
		.amdhsa_enable_private_segment 0
		.amdhsa_system_sgpr_workgroup_id_x 1
		.amdhsa_system_sgpr_workgroup_id_y 0
		.amdhsa_system_sgpr_workgroup_id_z 0
		.amdhsa_system_sgpr_workgroup_info 0
		.amdhsa_system_vgpr_workitem_id 0
		.amdhsa_next_free_vgpr 64
		.amdhsa_next_free_sgpr 70
		.amdhsa_accum_offset 64
		.amdhsa_reserve_vcc 1
		.amdhsa_float_round_mode_32 0
		.amdhsa_float_round_mode_16_64 0
		.amdhsa_float_denorm_mode_32 3
		.amdhsa_float_denorm_mode_16_64 3
		.amdhsa_dx10_clamp 1
		.amdhsa_ieee_mode 1
		.amdhsa_fp16_overflow 0
		.amdhsa_tg_split 0
		.amdhsa_exception_fp_ieee_invalid_op 0
		.amdhsa_exception_fp_denorm_src 0
		.amdhsa_exception_fp_ieee_div_zero 0
		.amdhsa_exception_fp_ieee_overflow 0
		.amdhsa_exception_fp_ieee_underflow 0
		.amdhsa_exception_fp_ieee_inexact 0
		.amdhsa_exception_int_div_zero 0
	.end_amdhsa_kernel

amdhsa.kernels:
  - .agpr_count:     0
    .args:
      - .actual_access:  read_only
        .address_space:  global
        .offset:         0
        .size:           8
        .value_kind:     global_buffer
      - .actual_access:  read_only
        .address_space:  global
        .offset:         8
        .size:           8
        .value_kind:     global_buffer
      - .actual_access:  read_only
        .address_space:  global
        .offset:         16
        .size:           8
        .value_kind:     global_buffer
      - .actual_access:  read_only
        .address_space:  global
        .offset:         24
        .size:           8
        .value_kind:     global_buffer
      - .actual_access:  read_only
        .address_space:  global
        .offset:         32
        .size:           8
        .value_kind:     global_buffer
      - .actual_access:  read_only
        .address_space:  global
        .offset:         40
        .size:           8
        .value_kind:     global_buffer
      - .actual_access:  write_only
        .address_space:  global
        .offset:         48
        .size:           8
        .value_kind:     global_buffer
      - .actual_access:  write_only
        .address_space:  global
        .offset:         56
        .size:           8
        .value_kind:     global_buffer
      - .actual_access:  write_only
        .address_space:  global
        .offset:         64
        .size:           8
        .value_kind:     global_buffer
      - .actual_access:  write_only
        .address_space:  global
        .offset:         72
        .size:           8
        .value_kind:     global_buffer
      - .actual_access:  write_only
        .address_space:  global
        .offset:         80
        .size:           8
        .value_kind:     global_buffer
    .group_segment_fixed_size: 20544
    .kernarg_segment_align: 8
    .kernarg_segment_size: 88
    .language:       OpenCL C
    .language_version:
      - 2
      - 0
    .max_flat_workgroup_size: 1024
    .name:           _Z6k_partPKiPKfS2_S2_S2_S2_PiS3_PDF16_S4_S4_
    .private_segment_fixed_size: 0
    .sgpr_count:     28
    .sgpr_spill_count: 0
    .symbol:         _Z6k_partPKiPKfS2_S2_S2_S2_PiS3_PDF16_S4_S4_.kd
    .uniform_work_group_size: 1
    .uses_dynamic_stack: false
    .vgpr_count:     44
    .vgpr_spill_count: 0
    .wavefront_size: 64
  - .agpr_count:     0
    .args:
      - .actual_access:  read_only
        .address_space:  global
        .offset:         0
        .size:           8
        .value_kind:     global_buffer
      - .actual_access:  read_only
        .address_space:  global
        .offset:         8
        .size:           8
        .value_kind:     global_buffer
      - .actual_access:  read_only
        .address_space:  global
        .offset:         16
        .size:           8
        .value_kind:     global_buffer
      - .actual_access:  write_only
        .address_space:  global
        .offset:         24
        .size:           8
        .value_kind:     global_buffer
      - .address_space:  global
        .offset:         32
        .size:           8
        .value_kind:     global_buffer
      - .actual_access:  read_only
        .address_space:  global
        .offset:         40
        .size:           8
        .value_kind:     global_buffer
      - .actual_access:  read_only
        .address_space:  global
        .offset:         48
        .size:           8
        .value_kind:     global_buffer
      - .actual_access:  read_only
        .address_space:  global
        .offset:         56
        .size:           8
        .value_kind:     global_buffer
      - .actual_access:  read_only
        .address_space:  global
        .offset:         64
        .size:           8
        .value_kind:     global_buffer
      - .actual_access:  write_only
        .address_space:  global
        .offset:         72
        .size:           8
        .value_kind:     global_buffer
      - .actual_access:  write_only
        .address_space:  global
        .offset:         80
        .size:           8
        .value_kind:     global_buffer
    .group_segment_fixed_size: 33712
    .kernarg_segment_align: 8
    .kernarg_segment_size: 88
    .language:       OpenCL C
    .language_version:
      - 2
      - 0
    .max_flat_workgroup_size: 512
    .name:           _Z8k_layer1PKDF16_PKiS2_PiS3_PKDv4_jS6_PKfS8_P15HIP_vector_typeIfLj2EESB_
    .private_segment_fixed_size: 0
    .sgpr_count:     76
    .sgpr_spill_count: 0
    .symbol:         _Z8k_layer1PKDF16_PKiS2_PiS3_PKDv4_jS6_PKfS8_P15HIP_vector_typeIfLj2EESB_.kd
    .uniform_work_group_size: 1
    .uses_dynamic_stack: false
    .vgpr_count:     64
    .vgpr_spill_count: 0
    .wavefront_size: 64
  - .agpr_count:     0
    .args:
      - .actual_access:  read_only
        .address_space:  global
        .offset:         0
        .size:           8
        .value_kind:     global_buffer
      - .actual_access:  read_only
        .address_space:  global
        .offset:         8
        .size:           8
        .value_kind:     global_buffer
      - .actual_access:  read_only
        .address_space:  global
        .offset:         16
        .size:           8
        .value_kind:     global_buffer
      - .actual_access:  read_only
        .address_space:  global
        .offset:         24
        .size:           8
        .value_kind:     global_buffer
      - .actual_access:  write_only
        .address_space:  global
        .offset:         32
        .size:           8
        .value_kind:     global_buffer
    .group_segment_fixed_size: 0
    .kernarg_segment_align: 8
    .kernarg_segment_size: 40
    .language:       OpenCL C
    .language_version:
      - 2
      - 0
    .max_flat_workgroup_size: 448
    .name:           _Z8k_layer2PK15HIP_vector_typeIfLj2EES2_PKiS4_PS0_
    .private_segment_fixed_size: 0
    .sgpr_count:     21
    .sgpr_spill_count: 0
    .symbol:         _Z8k_layer2PK15HIP_vector_typeIfLj2EES2_PKiS4_PS0_.kd
    .uniform_work_group_size: 1
    .uses_dynamic_stack: false
    .vgpr_count:     25
    .vgpr_spill_count: 0
    .wavefront_size: 64
